# dynamic-queue K1 + loads issued in 8KiB bursts (8 back-to-back 1KiB loads after 8 buffers are consumed), ring 16
# speedup vs baseline: 1.0764x; 1.0084x over previous
.Lk1_contm_7:
	global_load_dwordx4 v[28:31], v1, s[6:7] nt
	s_add_u32 s6, s6, 0x400
	s_addc_u32 s7, s7, 0
	global_load_dwordx4 v[32:35], v1, s[6:7] nt
	s_add_u32 s6, s6, 0x400
	s_addc_u32 s7, s7, 0
	global_load_dwordx4 v[36:39], v1, s[6:7] nt
	s_add_u32 s6, s6, 0x400
	s_addc_u32 s7, s7, 0
	global_load_dwordx4 v[40:43], v1, s[6:7] nt
	s_add_u32 s6, s6, 0x400
	s_addc_u32 s7, s7, 0
	global_load_dwordx4 v[44:47], v1, s[6:7] nt
	s_add_u32 s6, s6, 0x400
	s_addc_u32 s7, s7, 0
	global_load_dwordx4 v[48:51], v1, s[6:7] nt
	s_add_u32 s6, s6, 0x400
	s_addc_u32 s7, s7, 0
	global_load_dwordx4 v[52:55], v1, s[6:7] nt
	s_add_u32 s6, s6, 0x400
	s_addc_u32 s7, s7, 0
	global_load_dwordx4 v[56:59], v1, s[6:7] nt
	s_add_u32 s6, s6, 0x400
	s_addc_u32 s7, s7, 0
	s_waitcnt vmcnt(15)
	v_or3_b32 v12, v60, v61, v62
	v_or_b32_e32 v12, v12, v63
	v_cmp_ne_u32_e32 vcc, 0, v12
	s_cbranch_vccnz .Lk1_hitm_8
.Lk1_contm_8:
	s_waitcnt vmcnt(14)
	v_or3_b32 v12, v64, v65, v66
	v_or_b32_e32 v12, v12, v67
	v_cmp_ne_u32_e32 vcc, 0, v12
	s_cbranch_vccnz .Lk1_hitm_9
.Lk1_contm_9:
	s_waitcnt vmcnt(13)
	v_or3_b32 v12, v68, v69, v70
	v_or_b32_e32 v12, v12, v71
	v_cmp_ne_u32_e32 vcc, 0, v12
	s_cbranch_vccnz .Lk1_hitm_10
.Lk1_contm_10:
	s_waitcnt vmcnt(12)
	v_or3_b32 v12, v72, v73, v74
	v_or_b32_e32 v12, v12, v75
	v_cmp_ne_u32_e32 vcc, 0, v12
	s_cbranch_vccnz .Lk1_hitm_11
.Lk1_contm_11:
	s_waitcnt vmcnt(11)
	v_or3_b32 v12, v76, v77, v78
	v_or_b32_e32 v12, v12, v79
	v_cmp_ne_u32_e32 vcc, 0, v12
	s_cbranch_vccnz .Lk1_hitm_12
.Lk1_contm_12:
	s_waitcnt vmcnt(10)
	v_or3_b32 v12, v80, v81, v82
	v_or_b32_e32 v12, v12, v83
	v_cmp_ne_u32_e32 vcc, 0, v12
	s_cbranch_vccnz .Lk1_hitm_13
.Lk1_contm_13:
	s_waitcnt vmcnt(9)
	v_or3_b32 v12, v84, v85, v86
	v_or_b32_e32 v12, v12, v87
	v_cmp_ne_u32_e32 vcc, 0, v12
	s_cbranch_vccnz .Lk1_hitm_14
.Lk1_contm_14:
	s_waitcnt vmcnt(8)
	v_or3_b32 v12, v88, v89, v90
	v_or_b32_e32 v12, v12, v91
	v_cmp_ne_u32_e32 vcc, 0, v12
	s_cbranch_vccnz .Lk1_hitm_15
.Lk1_contm_15:
	global_load_dwordx4 v[60:63], v1, s[6:7] nt
	s_add_u32 s6, s6, 0x400
	s_addc_u32 s7, s7, 0
	global_load_dwordx4 v[64:67], v1, s[6:7] nt
	s_add_u32 s6, s6, 0x400
	s_addc_u32 s7, s7, 0
	global_load_dwordx4 v[68:71], v1, s[6:7] nt
	s_add_u32 s6, s6, 0x400
	s_addc_u32 s7, s7, 0
	global_load_dwordx4 v[72:75], v1, s[6:7] nt
	s_add_u32 s6, s6, 0x400
	s_addc_u32 s7, s7, 0
	global_load_dwordx4 v[76:79], v1, s[6:7] nt
	s_add_u32 s6, s6, 0x400
	s_addc_u32 s7, s7, 0
	global_load_dwordx4 v[80:83], v1, s[6:7] nt
	s_add_u32 s6, s6, 0x400
	s_addc_u32 s7, s7, 0
	global_load_dwordx4 v[84:87], v1, s[6:7] nt
	s_add_u32 s6, s6, 0x400
	s_addc_u32 s7, s7, 0
	global_load_dwordx4 v[88:91], v1, s[6:7] nt
	s_add_u32 s6, s6, 0x400
	s_addc_u32 s7, s7, 0
	s_mov_b32 s18, s58
	v_readfirstlane_b32 s56, v26
	s_nop 0
	s_add_u32 s56, s56, 256
	s_cmp_lt_u32 s56, 2304
	s_cbranch_scc0 .Lk1_lastchunk
	s_add_u32 s57, s52, s56
	s_mul_i32 s57, s57, 0x4000
	s_lshr_b32 s58, s57, 2
	s_add_u32 s6, s4, s57
	s_addc_u32 s7, s5, 0
	s_mov_b64 exec, 1
	global_atomic_add v26, v27, v21, s[54:55] sc0
	s_mov_b64 exec, -1
	s_branch .Lk1_main
